# placement check of v37: one s_nop at kernel entry moves the whole instruction stream by 4 bytes (every MFMA cluster at the other 8-byte phase)
# baseline (speedup 1.0000x reference)
; #define LAS __attribute__((address_space(3)))
; __global__ __launch_bounds__(NTHR, 2) void k_mega(Params p) {
;     LAS unsigned char* lds = (LAS unsigned char*)dynlds; LAS unsigned char* xl = lds + XL_OFF;
;     const int G = gridDim.x, c = blockIdx.x;
;     volatile LAS unsigned* xbw = (volatile LAS unsigned*)(lds + LDS_BYTES - 16);
;     if (threadIdx.x == 0) { xbw[0] = 0u; xbw[1] = 0u; xbw[2] = 0u; xbw[3] = 0u; }
;     __syncthreads();
;     const XcdBarrier bar = xcd_barrier_post((unsigned*)(p.ws + WS_CTL), xbw);
_Z6k_mega6Params:
	s_nop 0
	s_load_dword s94, s[0:1], 0xe0
	s_mov_b64 s[70:71], s[0:1]
	s_add_u32 s96, s70, 0xe0
	s_mov_b32 s92, s2
	s_addc_u32 s97, s71, 0
	v_cmp_eq_u32_e64 s[0:1], 0, v0
	s_mov_b64 s[6:7], exec
	s_nop 0
	v_writelane_b32 v240, s0, 0
	s_nop 1
	v_writelane_b32 v240, s1, 1
	s_and_b64 s[0:1], s[6:7], s[0:1]
	s_mov_b64 exec, s[0:1]
	s_cbranch_execz .LBB0_2
	s_add_i32 s0, 0, 0x25ff0
	v_mov_b32_e32 v1, 0
	v_mov_b32_e32 v2, s0
	s_add_i32 s0, 0, 0x25ff4
	ds_write_b32 v2, v1
	v_mov_b32_e32 v2, s0
	s_add_i32 s0, 0, 0x25ff8
	ds_write_b32 v2, v1
	v_mov_b32_e32 v2, s0
	s_add_i32 s0, 0, 0x25ffc
	ds_write_b32 v2, v1
	v_mov_b32_e32 v2, s0
	ds_write_b32 v2, v1
